# stack2: stack1 + write-through (sc1) stores for the final f32 output in the expert epilogue (no dirty output left in L2 at kernel end)
# baseline (speedup 1.0000x reference)
; DEVINL float bflo(unsigned u) { return __uint_as_float(u << 16); }
; DEVINL float bfhi(unsigned u) { return __uint_as_float(u & 0xffff0000u); }
; #define LDX1(mi_, buf_) { const int tk_ = s_tok[16 * (mi_) + lr2]; const bf16_t* xr_ = X1B + (size_t)(tk_ < 0 ? 0 : tk_) * DM + 128 * wv + 4 * g2; \
;                 _Pragma("unroll") for (int c_ = 0; c_ < 8; ++c_) xb[buf_][c_] = *(const u32x2*)(xr_ + 16 * c_); }
; DEVINL void phase5(const Params& P, unsigned char* smem) {
;     ...
;             LDX1(0, 0)
;             __syncthreads();
; #pragma unroll
;             for (int mi = 0; mi < 5; ++mi) {
;                 if (mi + 1 < 5) LDX1(mi + 1, (mi + 1) & 1)
;                 const int tok = s_tok[16 * mi + lr2];
;                 float qs = 0.f;
; #pragma unroll
;                 for (int w2 = 0; w2 < 8; ++w2) qs += s_part[w2 * 80 + 16 * mi + lr2];
;                 const float rstd = rsqrtf(qs * (1.f / DM) + EPS);
;                 const float* gfr = s_gfp + ((tok >> 13) & 1) * 1024 + 128 * wv + 4 * g2;
;                 float* orow = P.out + (size_t)(tok < 0 ? 0 : tok) * DM + 128 * wv + 4 * g2;
; #pragma unroll
;                 for (int c = 0; c < 8; ++c) {
;                     const f32x4 yv = c < 4 ? (f32x4){bflo(ypk[c & 3][mi].x), bfhi(ypk[c & 3][mi].x), bflo(ypk[c & 3][mi].y), bfhi(ypk[c & 3][mi].y)} : acc[c & 3][mi];
;                     const u32x2 xv = xb[mi & 1][c];
;                     const f32x4 x1 = {bflo(xv.x), bfhi(xv.x), bflo(xv.y), bfhi(xv.y)};
;                     const f32x4 gg = *(const f32x4*)(gfr + 16 * c);
;                     if (tok >= 0) *(f32x4*)(orow + 16 * c) = x1 + gg * (yv * rstd);
;                 }
.LBB0_730:
	s_or_b64 exec, exec, s[0:1]
	v_lshlrev_b32_e32 v140, 2, v225
	v_add_u32_e32 v54, 0, v140
	v_add_u32_e32 v175, 0x24900, v54
	ds_read_b32 v114, v175
	v_lshlrev_b32_e32 v54, 2, v224
	v_ashrrev_i32_e32 v55, 31, v54
	v_lshlrev_b64 v[92:93], 1, v[54:55]
	s_add_i32 s0, 0, 0x1e000
	s_waitcnt lgkmcnt(0)
	v_max_i32_e32 v194, 0, v114
	v_lshlrev_b64 v[114:115], 11, v[194:195]
	v_lshl_add_u64 v[114:115], s[10:11], 0, v[114:115]
	v_lshl_add_u64 v[114:115], v[114:115], 0, v[92:93]
	global_load_dwordx2 v[162:163], v[114:115], off
	global_load_dwordx2 v[160:161], v[114:115], off offset:32
	global_load_dwordx2 v[158:159], v[114:115], off offset:64
	global_load_dwordx2 v[156:157], v[114:115], off offset:96
	global_load_dwordx2 v[144:145], v[114:115], off offset:128
	global_load_dwordx2 v[124:125], v[114:115], off offset:160
	global_load_dwordx2 v[120:121], v[114:115], off offset:192
	global_load_dwordx2 v[116:117], v[114:115], off offset:224
	s_barrier
	ds_read2_b32 v[164:165], v175 offset1:16
	v_lshl_add_u64 v[92:93], s[10:11], 0, v[92:93]
	v_add_u32_e32 v177, s0, v140
	v_lshl_add_u32 v174, v224, 4, s33
	v_add_u32_e32 v176, 0x400, v177
	s_waitcnt lgkmcnt(0)
	v_max_i32_e32 v194, 0, v165
	v_lshlrev_b64 v[114:115], 11, v[194:195]
	v_lshl_add_u64 v[114:115], v[92:93], 0, v[114:115]
	global_load_dwordx2 v[154:155], v[114:115], off
	global_load_dwordx2 v[142:143], v[114:115], off offset:32
	global_load_dwordx2 v[138:139], v[114:115], off offset:64
	global_load_dwordx2 v[134:135], v[114:115], off offset:96
	global_load_dwordx2 v[130:131], v[114:115], off offset:128
	global_load_dwordx2 v[122:123], v[114:115], off offset:160
	global_load_dwordx2 v[118:119], v[114:115], off offset:192
	s_nop 0
	global_load_dwordx2 v[114:115], v[114:115], off offset:224
	v_cmp_lt_i32_e32 vcc, -1, v164
	v_add_u32_e32 v178, 0x600, v177
	s_and_saveexec_b64 s[0:1], vcc
	s_cbranch_execz .LBB0_732
	ds_read2_b32 v[140:141], v177 offset1:80
	ds_read2_b32 v[180:181], v177 offset0:160 offset1:240
	ds_read2_b32 v[182:183], v176 offset0:64 offset1:144
	v_cvt_pk_bf16_f32 v185, v204, v205
	v_cvt_pk_bf16_f32 v194, v210, v211
	s_waitcnt lgkmcnt(2)
	v_add_f32_e32 v140, 0, v140
	v_add_f32_e32 v165, v140, v141
	ds_read2_b32 v[140:141], v178 offset0:96 offset1:176
	s_waitcnt lgkmcnt(2)
	v_add_f32_e32 v165, v165, v180
	v_add_f32_e32 v165, v165, v181
	s_waitcnt lgkmcnt(1)
	v_add_f32_e32 v165, v165, v182
	v_add_f32_e32 v165, v165, v183
	s_waitcnt lgkmcnt(0)
	v_add_f32_e32 v140, v165, v140
	v_add_f32_e32 v140, v140, v141
	v_fmamk_f32 v140, v140, 0x3a800000, v221
	v_mul_f32_e32 v141, 0x4b800000, v140
	v_cmp_gt_f32_e32 vcc, s48, v140
	v_mov_b32_e32 v165, v195
	v_cvt_pk_bf16_f32 v210, v212, v213
	v_cndmask_b32_e32 v140, v140, v141, vcc
	v_rsq_f32_e32 v140, v140
	v_lshlrev_b32_e32 v180, 16, v185
	v_and_b32_e32 v181, 0xffff0000, v185
	v_cvt_pk_bf16_f32 v179, v206, v207
	v_mul_f32_e32 v141, 0x45800000, v140
	v_cndmask_b32_e32 v184, v140, v141, vcc
	v_lshlrev_b64 v[140:141], 12, v[164:165]
	v_lshrrev_b32_e32 v164, 1, v164
	v_and_b32_e32 v164, 0x1000, v164
	v_add_u32_e32 v213, v174, v164
	v_pk_mul_f32 v[188:189], v[184:185], v[180:181] op_sel_hi:[0,1]
	ds_read_b128 v[180:183], v213
	v_lshlrev_b32_e32 v164, 16, v179
	v_and_b32_e32 v165, 0xffff0000, v179
	v_pk_mul_f32 v[186:187], v[184:185], v[164:165] op_sel_hi:[0,1]
	s_waitcnt vmcnt(15)
	v_and_b32_e32 v205, 0xffff0000, v163
	v_lshlrev_b32_e32 v206, 16, v162
	v_and_b32_e32 v207, 0xffff0000, v162
	v_lshlrev_b32_e32 v204, 16, v163
	ds_read_b128 v[162:165], v213 offset:64
	v_lshl_add_u64 v[140:141], s[12:13], 0, v[140:141]
	v_cvt_pk_bf16_f32 v208, v208, v209
	v_lshl_add_u64 v[140:141], v[54:55], 2, v[140:141]
	s_waitcnt lgkmcnt(1)
	v_pk_fma_f32 v[182:183], v[182:183], v[188:189], v[204:205]
	v_pk_fma_f32 v[180:181], v[180:181], v[186:187], v[206:207]
	global_store_dwordx4 v[140:141], v[180:183], off sc1
	s_waitcnt vmcnt(15)
	v_and_b32_e32 v187, 0xffff0000, v161
	v_lshlrev_b32_e32 v188, 16, v160
	v_lshlrev_b32_e32 v180, 16, v194
	v_and_b32_e32 v181, 0xffff0000, v194
	v_lshlrev_b32_e32 v182, 16, v208
	v_and_b32_e32 v183, 0xffff0000, v208
	v_pk_mul_f32 v[180:181], v[184:185], v[180:181] op_sel_hi:[0,1]
	v_pk_mul_f32 v[182:183], v[184:185], v[182:183] op_sel_hi:[0,1]
	v_and_b32_e32 v189, 0xffff0000, v160
	v_lshlrev_b32_e32 v186, 16, v161
	v_cvt_pk_bf16_f32 v209, v214, v215
	s_waitcnt lgkmcnt(0)
	v_pk_fma_f32 v[164:165], v[164:165], v[182:183], v[186:187]
	v_pk_fma_f32 v[162:163], v[162:163], v[180:181], v[188:189]
	global_store_dwordx4 v[140:141], v[162:165], off offset:64 sc1
	v_lshlrev_b32_e32 v160, 16, v209
	v_and_b32_e32 v161, 0xffff0000, v209
	v_lshlrev_b32_e32 v162, 16, v210
	v_and_b32_e32 v163, 0xffff0000, v210
	v_pk_mul_f32 v[164:165], v[184:185], v[160:161] op_sel_hi:[0,1]
	v_pk_mul_f32 v[186:187], v[184:185], v[162:163] op_sel_hi:[0,1]
	ds_read_b128 v[160:163], v213 offset:128
	ds_read_b128 v[180:183], v213 offset:192
	s_waitcnt vmcnt(15)
	v_and_b32_e32 v189, 0xffff0000, v159
	v_lshlrev_b32_e32 v204, 16, v158
	v_and_b32_e32 v205, 0xffff0000, v158
	v_lshlrev_b32_e32 v188, 16, v159
	v_cvt_pk_bf16_f32 v211, v218, v219
	v_cvt_pk_bf16_f32 v212, v216, v217
	s_waitcnt lgkmcnt(1)
	v_pk_fma_f32 v[162:163], v[162:163], v[186:187], v[188:189]
	v_pk_fma_f32 v[160:161], v[160:161], v[164:165], v[204:205]
	global_store_dwordx4 v[140:141], v[160:163], off offset:128 sc1
	v_lshlrev_b32_e32 v158, 16, v211
	v_and_b32_e32 v159, 0xffff0000, v211
	v_lshlrev_b32_e32 v160, 16, v212
	v_and_b32_e32 v161, 0xffff0000, v212
	v_pk_mul_f32 v[162:163], v[184:185], v[158:159] op_sel_hi:[0,1]
	v_pk_mul_f32 v[158:159], v[184:185], v[160:161] op_sel_hi:[0,1]
	s_waitcnt vmcnt(15)
; DEVINL float bflo(unsigned u) { return __uint_as_float(u << 16); }
; DEVINL float bfhi(unsigned u) { return __uint_as_float(u & 0xffff0000u); }
; #define LDX1(mi_, buf_) { const int tk_ = s_tok[16 * (mi_) + lr2]; const bf16_t* xr_ = X1B + (size_t)(tk_ < 0 ? 0 : tk_) * DM + 128 * wv + 4 * g2; \
;                 _Pragma("unroll") for (int c_ = 0; c_ < 8; ++c_) xb[buf_][c_] = *(const u32x2*)(xr_ + 16 * c_); }
; DEVINL void phase5(const Params& P, unsigned char* smem) {
;     ...
;             for (int mi = 0; mi < 5; ++mi) {
;                 if (mi + 1 < 5) LDX1(mi + 1, (mi + 1) & 1)
;                 const int tok = s_tok[16 * mi + lr2];
;                 float qs = 0.f;
; #pragma unroll
;                 for (int w2 = 0; w2 < 8; ++w2) qs += s_part[w2 * 80 + 16 * mi + lr2];
;                 const float rstd = rsqrtf(qs * (1.f / DM) + EPS);
;                 const float* gfr = s_gfp + ((tok >> 13) & 1) * 1024 + 128 * wv + 4 * g2;
;                 float* orow = P.out + (size_t)(tok < 0 ? 0 : tok) * DM + 128 * wv + 4 * g2;
; #pragma unroll
;                 for (int c = 0; c < 8; ++c) {
;                     const f32x4 yv = c < 4 ? (f32x4){bflo(ypk[c & 3][mi].x), bfhi(ypk[c & 3][mi].x), bflo(ypk[c & 3][mi].y), bfhi(ypk[c & 3][mi].y)} : acc[c & 3][mi];
;                     const u32x2 xv = xb[mi & 1][c];
;                     const f32x4 x1 = {bflo(xv.x), bfhi(xv.x), bflo(xv.y), bfhi(xv.y)};
;                     const f32x4 gg = *(const f32x4*)(gfr + 16 * c);
;                     if (tok >= 0) *(f32x4*)(orow + 16 * c) = x1 + gg * (yv * rstd);
;                 }
	v_and_b32_e32 v161, 0xffff0000, v157
	v_lshlrev_b32_e32 v164, 16, v156
	v_and_b32_e32 v165, 0xffff0000, v156
	v_lshlrev_b32_e32 v160, 16, v157
	s_waitcnt lgkmcnt(0)
	v_pk_fma_f32 v[158:159], v[182:183], v[158:159], v[160:161]
	v_pk_fma_f32 v[156:157], v[180:181], v[162:163], v[164:165]
	global_store_dwordx4 v[140:141], v[156:159], off offset:192 sc1
	ds_read_b128 v[156:159], v213 offset:256
	ds_read_b128 v[160:163], v213 offset:320
	v_pk_mul_f32 v[164:165], v[192:193], v[184:185] op_sel_hi:[1,0]
	v_pk_mul_f32 v[180:181], v[190:191], v[184:185] op_sel_hi:[1,0]
	s_waitcnt vmcnt(15)
	v_and_b32_e32 v183, 0xffff0000, v145
	v_lshlrev_b32_e32 v186, 16, v144
	v_and_b32_e32 v187, 0xffff0000, v144
	v_lshlrev_b32_e32 v182, 16, v145
	s_waitcnt lgkmcnt(1)
	v_pk_fma_f32 v[156:157], v[156:157], v[180:181], v[186:187]
	v_pk_fma_f32 v[158:159], v[158:159], v[164:165], v[182:183]
	global_store_dwordx4 v[140:141], v[156:159], off offset:256 sc1
	v_pk_mul_f32 v[144:145], v[172:173], v[184:185] op_sel_hi:[1,0]
	s_waitcnt vmcnt(15)
	v_lshlrev_b32_e32 v164, 16, v124
	v_pk_mul_f32 v[156:157], v[170:171], v[184:185] op_sel_hi:[1,0]
	v_and_b32_e32 v159, 0xffff0000, v125
	v_and_b32_e32 v165, 0xffff0000, v124
	v_lshlrev_b32_e32 v158, 16, v125
	s_waitcnt lgkmcnt(0)
	v_pk_fma_f32 v[156:157], v[156:157], v[160:161], v[164:165]
	v_pk_fma_f32 v[158:159], v[144:145], v[162:163], v[158:159]
	v_pk_mul_f32 v[124:125], v[152:153], v[184:185] op_sel_hi:[1,0]
	v_pk_mul_f32 v[144:145], v[150:151], v[184:185] op_sel_hi:[1,0]
	ds_read_b128 v[150:153], v213 offset:384
	global_store_dwordx4 v[140:141], v[156:159], off offset:320 sc1
	ds_read_b128 v[156:159], v213 offset:448
	s_waitcnt vmcnt(15)
	v_and_b32_e32 v161, 0xffff0000, v121
	v_lshlrev_b32_e32 v162, 16, v120
	v_and_b32_e32 v163, 0xffff0000, v120
	v_lshlrev_b32_e32 v160, 16, v121
	s_waitcnt lgkmcnt(1)
	v_pk_fma_f32 v[150:151], v[144:145], v[150:151], v[162:163]
	v_pk_fma_f32 v[152:153], v[124:125], v[152:153], v[160:161]
	v_pk_mul_f32 v[120:121], v[132:133], v[184:185] op_sel_hi:[1,0]
	v_pk_mul_f32 v[124:125], v[136:137], v[184:185] op_sel_hi:[1,0]
	s_waitcnt vmcnt(14)
	v_and_b32_e32 v133, 0xffff0000, v117
	v_lshlrev_b32_e32 v136, 16, v116
	v_and_b32_e32 v137, 0xffff0000, v116
	v_lshlrev_b32_e32 v132, 16, v117
	global_store_dwordx4 v[140:141], v[150:153], off offset:384 sc1
	s_waitcnt lgkmcnt(0)
	s_nop 0
	v_pk_fma_f32 v[150:151], v[124:125], v[156:157], v[136:137]
	v_pk_fma_f32 v[152:153], v[120:121], v[158:159], v[132:133]
	global_store_dwordx4 v[140:141], v[150:153], off offset:448 sc1
.LBB0_732:
	s_or_b64 exec, exec, s[0:1]
	ds_read2_b32 v[152:153], v175 offset0:16 offset1:32
	s_waitcnt vmcnt(12)
	v_add_u32_e32 v156, 0x200, v177
	s_waitcnt lgkmcnt(0)
	v_max_i32_e32 v194, 0, v153
	s_waitcnt vmcnt(8)
	v_lshlrev_b64 v[116:117], 11, v[194:195]
	v_lshl_add_u64 v[116:117], v[92:93], 0, v[116:117]
	global_load_dwordx2 v[150:151], v[116:117], off
	global_load_dwordx2 v[144:145], v[116:117], off offset:32
	global_load_dwordx2 v[140:141], v[116:117], off offset:64
	global_load_dwordx2 v[136:137], v[116:117], off offset:96
	global_load_dwordx2 v[132:133], v[116:117], off offset:128
	global_load_dwordx2 v[124:125], v[116:117], off offset:160
	global_load_dwordx2 v[120:121], v[116:117], off offset:192
	s_nop 0
	global_load_dwordx2 v[116:117], v[116:117], off offset:224
	v_cmp_lt_i32_e32 vcc, -1, v152
	s_and_saveexec_b64 s[0:1], vcc
	s_cbranch_execz .LBB0_734
	v_cvt_pk_bf16_f32 v157, v106, v107
	ds_read2_b32 v[106:107], v177 offset0:16 offset1:96
	v_cvt_pk_bf16_f32 v171, v94, v95
	ds_read2_b32 v[94:95], v156 offset0:48 offset1:128
	v_cvt_pk_bf16_f32 v170, v96, v97
	ds_read2_b32 v[96:97], v176 offset0:80 offset1:160
	s_waitcnt lgkmcnt(2)
	v_add_f32_e32 v106, 0, v106
	v_cvt_pk_bf16_f32 v109, v108, v109
	v_add_f32_e32 v108, v106, v107
	ds_read2_b32 v[106:107], v178 offset0:112 offset1:192
	s_waitcnt lgkmcnt(2)
	v_add_f32_e32 v94, v108, v94
	v_add_f32_e32 v94, v94, v95
	s_waitcnt lgkmcnt(1)
	v_add_f32_e32 v94, v94, v96
	v_add_f32_e32 v94, v94, v97
	s_waitcnt lgkmcnt(0)
	v_add_f32_e32 v94, v94, v106
	v_add_f32_e32 v94, v94, v107
	v_fmamk_f32 v94, v94, 0x3a800000, v221
	v_mul_f32_e32 v95, 0x4b800000, v94
	v_cmp_gt_f32_e32 vcc, s48, v94
	v_lshrrev_b32_e32 v106, 1, v152
	v_and_b32_e32 v106, 0x1000, v106
	v_cndmask_b32_e32 v94, v94, v95, vcc
	v_rsq_f32_e32 v94, v94
	v_cvt_pk_bf16_f32 v97, v196, v197
	v_add_u32_e32 v179, v174, v106
	v_lshlrev_b32_e32 v106, 16, v157
	v_mul_f32_e32 v95, 0x45800000, v94
	v_cndmask_b32_e32 v96, v94, v95, vcc
	v_and_b32_e32 v107, 0xffff0000, v157
	v_lshlrev_b32_e32 v108, 16, v109
	v_and_b32_e32 v109, 0xffff0000, v109
	v_pk_mul_f32 v[158:159], v[96:97], v[106:107] op_sel_hi:[0,1]
	v_pk_mul_f32 v[160:161], v[96:97], v[108:109] op_sel_hi:[0,1]
	ds_read_b128 v[106:109], v179
	v_mov_b32_e32 v153, v195
	v_lshlrev_b64 v[94:95], 12, v[152:153]
	s_waitcnt vmcnt(15)
	v_and_b32_e32 v163, 0xffff0000, v155
	v_lshlrev_b32_e32 v164, 16, v154
	v_and_b32_e32 v165, 0xffff0000, v154
	v_lshlrev_b32_e32 v162, 16, v155
	ds_read_b128 v[152:155], v179 offset:64
	v_lshl_add_u64 v[94:95], s[12:13], 0, v[94:95]
	v_lshl_add_u64 v[94:95], v[54:55], 2, v[94:95]
	s_waitcnt lgkmcnt(1)
	v_pk_fma_f32 v[108:109], v[108:109], v[160:161], v[162:163]
	v_pk_fma_f32 v[106:107], v[106:107], v[158:159], v[164:165]
	global_store_dwordx4 v[94:95], v[106:109], off sc1
	s_waitcnt vmcnt(15)
	v_and_b32_e32 v159, 0xffff0000, v143
	v_lshlrev_b32_e32 v160, 16, v142
	v_lshlrev_b32_e32 v106, 16, v170
	v_and_b32_e32 v107, 0xffff0000, v170
	v_lshlrev_b32_e32 v108, 16, v171
	v_and_b32_e32 v109, 0xffff0000, v171
	v_pk_mul_f32 v[106:107], v[96:97], v[106:107] op_sel_hi:[0,1]
	v_pk_mul_f32 v[108:109], v[96:97], v[108:109] op_sel_hi:[0,1]
	v_and_b32_e32 v161, 0xffff0000, v142
	v_lshlrev_b32_e32 v158, 16, v143
	v_cvt_pk_bf16_f32 v172, v198, v199
	s_waitcnt lgkmcnt(0)
; DEVINL float bflo(unsigned u) { return __uint_as_float(u << 16); }
; DEVINL float bfhi(unsigned u) { return __uint_as_float(u & 0xffff0000u); }
; #define LDX1(mi_, buf_) { const int tk_ = s_tok[16 * (mi_) + lr2]; const bf16_t* xr_ = X1B + (size_t)(tk_ < 0 ? 0 : tk_) * DM + 128 * wv + 4 * g2; \
;                 _Pragma("unroll") for (int c_ = 0; c_ < 8; ++c_) xb[buf_][c_] = *(const u32x2*)(xr_ + 16 * c_); }
; DEVINL void phase5(const Params& P, unsigned char* smem) {
;     ...
;             for (int mi = 0; mi < 5; ++mi) {
;                 if (mi + 1 < 5) LDX1(mi + 1, (mi + 1) & 1)
;                 const int tok = s_tok[16 * mi + lr2];
;                 float qs = 0.f;
; #pragma unroll
;                 for (int w2 = 0; w2 < 8; ++w2) qs += s_part[w2 * 80 + 16 * mi + lr2];
;                 const float rstd = rsqrtf(qs * (1.f / DM) + EPS);
;                 const float* gfr = s_gfp + ((tok >> 13) & 1) * 1024 + 128 * wv + 4 * g2;
;                 float* orow = P.out + (size_t)(tok < 0 ? 0 : tok) * DM + 128 * wv + 4 * g2;
; #pragma unroll
;                 for (int c = 0; c < 8; ++c) {
;                     const f32x4 yv = c < 4 ? (f32x4){bflo(ypk[c & 3][mi].x), bfhi(ypk[c & 3][mi].x), bflo(ypk[c & 3][mi].y), bfhi(ypk[c & 3][mi].y)} : acc[c & 3][mi];
;                     const u32x2 xv = xb[mi & 1][c];
;                     const f32x4 x1 = {bflo(xv.x), bfhi(xv.x), bflo(xv.y), bfhi(xv.y)};
;                     const f32x4 gg = *(const f32x4*)(gfr + 16 * c);
;                     if (tok >= 0) *(f32x4*)(orow + 16 * c) = x1 + gg * (yv * rstd);
;                 }
	v_pk_fma_f32 v[108:109], v[154:155], v[108:109], v[158:159]
	v_pk_fma_f32 v[106:107], v[152:153], v[106:107], v[160:161]
	global_store_dwordx4 v[94:95], v[106:109], off offset:64 sc1
	ds_read_b128 v[152:155], v179 offset:192
	s_waitcnt vmcnt(15)
	v_and_b32_e32 v161, 0xffff0000, v139
	v_lshlrev_b32_e32 v106, 16, v172
	v_and_b32_e32 v107, 0xffff0000, v172
	v_lshlrev_b32_e32 v108, 16, v97
	v_and_b32_e32 v109, 0xffff0000, v97
	v_pk_mul_f32 v[142:143], v[96:97], v[106:107] op_sel_hi:[0,1]
	v_pk_mul_f32 v[158:159], v[96:97], v[108:109] op_sel_hi:[0,1]
	ds_read_b128 v[106:109], v179 offset:128
	v_lshlrev_b32_e32 v162, 16, v138
	v_and_b32_e32 v163, 0xffff0000, v138
	v_lshlrev_b32_e32 v160, 16, v139
	v_cvt_pk_bf16_f32 v173, v202, v203
	v_cvt_pk_bf16_f32 v178, v200, v201
	s_waitcnt lgkmcnt(0)
	v_pk_fma_f32 v[108:109], v[108:109], v[158:159], v[160:161]
	v_pk_fma_f32 v[106:107], v[106:107], v[142:143], v[162:163]
	global_store_dwordx4 v[94:95], v[106:109], off offset:128 sc1
	s_waitcnt vmcnt(15)
	v_and_b32_e32 v139, 0xffff0000, v135
	v_lshlrev_b32_e32 v142, 16, v134
	v_lshlrev_b32_e32 v106, 16, v173
	v_and_b32_e32 v107, 0xffff0000, v173
	v_lshlrev_b32_e32 v108, 16, v178
	v_and_b32_e32 v109, 0xffff0000, v178
	v_pk_mul_f32 v[106:107], v[96:97], v[106:107] op_sel_hi:[0,1]
	v_pk_mul_f32 v[108:109], v[96:97], v[108:109] op_sel_hi:[0,1]
	v_and_b32_e32 v143, 0xffff0000, v134
	v_lshlrev_b32_e32 v138, 16, v135
	v_pk_fma_f32 v[108:109], v[154:155], v[108:109], v[138:139]
	v_pk_fma_f32 v[106:107], v[152:153], v[106:107], v[142:143]
	global_store_dwordx4 v[94:95], v[106:109], off offset:192 sc1
	ds_read_b128 v[106:109], v179 offset:256
	v_pk_mul_f32 v[134:135], v[110:111], v[96:97] op_sel_hi:[1,0]
	v_pk_mul_f32 v[138:139], v[112:113], v[96:97] op_sel_hi:[1,0]
	ds_read_b128 v[110:113], v179 offset:320
	s_waitcnt vmcnt(15)
	v_and_b32_e32 v143, 0xffff0000, v131
	v_lshlrev_b32_e32 v152, 16, v130
	v_and_b32_e32 v153, 0xffff0000, v130
	v_lshlrev_b32_e32 v142, 16, v131
	s_waitcnt lgkmcnt(1)
	v_pk_fma_f32 v[106:107], v[106:107], v[138:139], v[152:153]
	v_pk_fma_f32 v[108:109], v[108:109], v[134:135], v[142:143]
	global_store_dwordx4 v[94:95], v[106:109], off offset:256 sc1
	s_waitcnt vmcnt(15)
	v_and_b32_e32 v131, 0xffff0000, v123
	v_lshlrev_b32_e32 v134, 16, v122
	v_pk_mul_f32 v[108:109], v[168:169], v[96:97] op_sel_hi:[1,0]
	v_pk_mul_f32 v[106:107], v[166:167], v[96:97] op_sel_hi:[1,0]
	v_and_b32_e32 v135, 0xffff0000, v122
	v_lshlrev_b32_e32 v130, 16, v123
	s_waitcnt lgkmcnt(0)
	v_pk_fma_f32 v[106:107], v[106:107], v[110:111], v[134:135]
	v_pk_fma_f32 v[108:109], v[108:109], v[112:113], v[130:131]
	global_store_dwordx4 v[94:95], v[106:109], off offset:320 sc1
	ds_read_b128 v[106:109], v179 offset:384
	ds_read_b128 v[110:113], v179 offset:448
	v_pk_mul_f32 v[122:123], v[148:149], v[96:97] op_sel_hi:[1,0]
	v_pk_mul_f32 v[130:131], v[146:147], v[96:97] op_sel_hi:[1,0]
	s_waitcnt vmcnt(15)
	v_and_b32_e32 v135, 0xffff0000, v119
	v_lshlrev_b32_e32 v138, 16, v118
	v_and_b32_e32 v139, 0xffff0000, v118
	v_lshlrev_b32_e32 v134, 16, v119
	s_waitcnt lgkmcnt(1)
	v_pk_fma_f32 v[106:107], v[130:131], v[106:107], v[138:139]
	v_pk_fma_f32 v[108:109], v[122:123], v[108:109], v[134:135]
	global_store_dwordx4 v[94:95], v[106:109], off offset:384 sc1
	s_waitcnt vmcnt(15)
	v_and_b32_e32 v119, 0xffff0000, v115
	v_lshlrev_b32_e32 v118, 16, v115
	v_pk_mul_f32 v[108:109], v[128:129], v[96:97] op_sel_hi:[1,0]
	v_pk_mul_f32 v[96:97], v[126:127], v[96:97] op_sel_hi:[1,0]
	v_lshlrev_b32_e32 v106, 16, v114
	v_and_b32_e32 v107, 0xffff0000, v114
	s_waitcnt lgkmcnt(0)
	v_pk_fma_f32 v[106:107], v[96:97], v[110:111], v[106:107]
	v_pk_fma_f32 v[108:109], v[108:109], v[112:113], v[118:119]
	global_store_dwordx4 v[94:95], v[106:109], off offset:448 sc1
.LBB0_734:
	s_or_b64 exec, exec, s[0:1]
	s_waitcnt vmcnt(10)
	ds_read2_b32 v[122:123], v175 offset0:32 offset1:48
	v_add_u32_e32 v126, 0x800, v177
	s_waitcnt lgkmcnt(0)
	v_max_i32_e32 v194, 0, v123
	v_lshlrev_b64 v[94:95], 11, v[194:195]
	v_lshl_add_u64 v[94:95], v[92:93], 0, v[94:95]
	global_load_dwordx2 v[118:119], v[94:95], off
	global_load_dwordx2 v[114:115], v[94:95], off offset:32
	global_load_dwordx2 v[112:113], v[94:95], off offset:64
	global_load_dwordx2 v[110:111], v[94:95], off offset:96
	global_load_dwordx2 v[108:109], v[94:95], off offset:128
	global_load_dwordx2 v[106:107], v[94:95], off offset:160
	global_load_dwordx2 v[96:97], v[94:95], off offset:192
	s_nop 0
	global_load_dwordx2 v[94:95], v[94:95], off offset:224
	v_cmp_lt_i32_e32 vcc, -1, v122
	s_and_saveexec_b64 s[0:1], vcc
	s_cbranch_execz .LBB0_736
; DEVINL float bflo(unsigned u) { return __uint_as_float(u << 16); }
; DEVINL float bfhi(unsigned u) { return __uint_as_float(u & 0xffff0000u); }
; #define LDX1(mi_, buf_) { const int tk_ = s_tok[16 * (mi_) + lr2]; const bf16_t* xr_ = X1B + (size_t)(tk_ < 0 ? 0 : tk_) * DM + 128 * wv + 4 * g2; \
;                 _Pragma("unroll") for (int c_ = 0; c_ < 8; ++c_) xb[buf_][c_] = *(const u32x2*)(xr_ + 16 * c_); }
; DEVINL void phase5(const Params& P, unsigned char* smem) {
;     ...
;             for (int mi = 0; mi < 5; ++mi) {
;                 if (mi + 1 < 5) LDX1(mi + 1, (mi + 1) & 1)
;                 const int tok = s_tok[16 * mi + lr2];
;                 float qs = 0.f;
; #pragma unroll
;                 for (int w2 = 0; w2 < 8; ++w2) qs += s_part[w2 * 80 + 16 * mi + lr2];
;                 const float rstd = rsqrtf(qs * (1.f / DM) + EPS);
;                 const float* gfr = s_gfp + ((tok >> 13) & 1) * 1024 + 128 * wv + 4 * g2;
;                 float* orow = P.out + (size_t)(tok < 0 ? 0 : tok) * DM + 128 * wv + 4 * g2;
; #pragma unroll
;                 for (int c = 0; c < 8; ++c) {
;                     const f32x4 yv = c < 4 ? (f32x4){bflo(ypk[c & 3][mi].x), bfhi(ypk[c & 3][mi].x), bflo(ypk[c & 3][mi].y), bfhi(ypk[c & 3][mi].y)} : acc[c & 3][mi];
;                     const u32x2 xv = xb[mi & 1][c];
;                     const f32x4 x1 = {bflo(xv.x), bfhi(xv.x), bflo(xv.y), bfhi(xv.y)};
;                     const f32x4 gg = *(const f32x4*)(gfr + 16 * c);
;                     if (tok >= 0) *(f32x4*)(orow + 16 * c) = x1 + gg * (yv * rstd);
;                 }
	v_cvt_pk_bf16_f32 v127, v102, v103
	ds_read2_b32 v[102:103], v177 offset0:32 offset1:112
	v_cvt_pk_bf16_f32 v134, v70, v71
	ds_read2_b32 v[70:71], v156 offset0:64 offset1:144
	v_cvt_pk_bf16_f32 v130, v82, v83
	ds_read2_b32 v[82:83], v176 offset0:96 offset1:176
	v_cvt_pk_bf16_f32 v131, v84, v85
	s_waitcnt lgkmcnt(2)
	v_add_f32_e32 v84, 0, v102
	v_add_f32_e32 v102, v84, v103
	ds_read2_b32 v[84:85], v126 offset1:80
	s_waitcnt lgkmcnt(2)
	v_add_f32_e32 v70, v102, v70
	v_add_f32_e32 v70, v70, v71
	s_waitcnt lgkmcnt(1)
	v_add_f32_e32 v70, v70, v82
	v_add_f32_e32 v70, v70, v83
	s_waitcnt lgkmcnt(0)
	v_add_f32_e32 v70, v70, v84
	v_add_f32_e32 v70, v70, v85
	v_fmamk_f32 v70, v70, 0x3a800000, v221
	v_mul_f32_e32 v71, 0x4b800000, v70
	v_cmp_gt_f32_e32 vcc, s48, v70
	v_cvt_pk_bf16_f32 v135, v64, v65
	v_cvt_pk_bf16_f32 v75, v74, v75
	v_cndmask_b32_e32 v70, v70, v71, vcc
	v_rsq_f32_e32 v70, v70
	v_cvt_pk_bf16_f32 v104, v104, v105
	v_cvt_pk_bf16_f32 v138, v72, v73
	v_and_b32_e32 v71, 0xffff0000, v127
	v_mul_f32_e32 v64, 0x45800000, v70
	v_cndmask_b32_e32 v74, v70, v64, vcc
	v_lshrrev_b32_e32 v70, 1, v122
	v_and_b32_e32 v70, 0x1000, v70
	v_add_u32_e32 v139, v174, v70
	v_lshlrev_b32_e32 v70, 16, v127
	v_lshlrev_b32_e32 v72, 16, v104
	v_and_b32_e32 v73, 0xffff0000, v104
	v_pk_mul_f32 v[102:103], v[74:75], v[70:71] op_sel_hi:[0,1]
	v_pk_mul_f32 v[104:105], v[74:75], v[72:73] op_sel_hi:[0,1]
	ds_read_b128 v[70:73], v139
	ds_read_b128 v[82:85], v139 offset:64
	v_mov_b32_e32 v123, v195
	v_lshlrev_b64 v[64:65], 12, v[122:123]
	v_lshl_add_u64 v[64:65], s[12:13], 0, v[64:65]
	s_waitcnt vmcnt(15)
	v_and_b32_e32 v123, 0xffff0000, v151
	v_lshlrev_b32_e32 v128, 16, v150
	v_and_b32_e32 v129, 0xffff0000, v150
	v_lshlrev_b32_e32 v122, 16, v151
	v_lshl_add_u64 v[64:65], v[54:55], 2, v[64:65]
	s_waitcnt lgkmcnt(1)
	v_pk_fma_f32 v[72:73], v[72:73], v[104:105], v[122:123]
	v_pk_fma_f32 v[70:71], v[70:71], v[102:103], v[128:129]
	global_store_dwordx4 v[64:65], v[70:73], off sc1
	s_waitcnt vmcnt(15)
	v_and_b32_e32 v103, 0xffff0000, v145
	v_lshlrev_b32_e32 v104, 16, v144
	v_lshlrev_b32_e32 v70, 16, v130
	v_and_b32_e32 v71, 0xffff0000, v130
	v_lshlrev_b32_e32 v72, 16, v131
	v_and_b32_e32 v73, 0xffff0000, v131
	v_pk_mul_f32 v[70:71], v[74:75], v[70:71] op_sel_hi:[0,1]
	v_pk_mul_f32 v[72:73], v[74:75], v[72:73] op_sel_hi:[0,1]
	v_and_b32_e32 v105, 0xffff0000, v144
	v_lshlrev_b32_e32 v102, 16, v145
	s_waitcnt lgkmcnt(0)
	v_pk_fma_f32 v[72:73], v[84:85], v[72:73], v[102:103]
	v_pk_fma_f32 v[70:71], v[82:83], v[70:71], v[104:105]
	global_store_dwordx4 v[64:65], v[70:73], off offset:64 sc1
	ds_read_b128 v[82:85], v139 offset:192
	s_waitcnt vmcnt(15)
	v_and_b32_e32 v123, 0xffff0000, v141
	v_lshlrev_b32_e32 v70, 16, v134
	v_and_b32_e32 v71, 0xffff0000, v134
	v_lshlrev_b32_e32 v72, 16, v135
	v_and_b32_e32 v73, 0xffff0000, v135
	v_pk_mul_f32 v[102:103], v[74:75], v[70:71] op_sel_hi:[0,1]
	v_pk_mul_f32 v[104:105], v[74:75], v[72:73] op_sel_hi:[0,1]
	ds_read_b128 v[70:73], v139 offset:128
	v_lshlrev_b32_e32 v128, 16, v140
	v_and_b32_e32 v129, 0xffff0000, v140
	v_lshlrev_b32_e32 v122, 16, v141
	v_pk_mul_f32 v[56:57], v[56:57], v[74:75] op_sel_hi:[1,0]
	s_waitcnt lgkmcnt(0)
	v_pk_fma_f32 v[72:73], v[72:73], v[104:105], v[122:123]
	v_pk_fma_f32 v[70:71], v[70:71], v[102:103], v[128:129]
	global_store_dwordx4 v[64:65], v[70:73], off offset:128 sc1
	s_waitcnt vmcnt(15)
	v_and_b32_e32 v103, 0xffff0000, v137
	v_lshlrev_b32_e32 v104, 16, v136
	v_lshlrev_b32_e32 v70, 16, v75
	v_and_b32_e32 v71, 0xffff0000, v75
	v_lshlrev_b32_e32 v72, 16, v138
	v_and_b32_e32 v73, 0xffff0000, v138
	v_pk_mul_f32 v[70:71], v[74:75], v[70:71] op_sel_hi:[0,1]
	v_pk_mul_f32 v[72:73], v[74:75], v[72:73] op_sel_hi:[0,1]
	v_and_b32_e32 v105, 0xffff0000, v136
	v_lshlrev_b32_e32 v102, 16, v137
	v_pk_fma_f32 v[72:73], v[84:85], v[72:73], v[102:103]
	v_pk_fma_f32 v[70:71], v[82:83], v[70:71], v[104:105]
	global_store_dwordx4 v[64:65], v[70:73], off offset:192 sc1
	ds_read_b128 v[70:73], v139 offset:256
	ds_read_b128 v[82:85], v139 offset:320
	v_pk_mul_f32 v[62:63], v[62:63], v[74:75] op_sel_hi:[1,0]
	s_waitcnt vmcnt(15)
	v_and_b32_e32 v103, 0xffff0000, v133
	v_lshlrev_b32_e32 v104, 16, v132
	v_and_b32_e32 v105, 0xffff0000, v132
	v_lshlrev_b32_e32 v102, 16, v133
	s_waitcnt lgkmcnt(1)
	v_pk_fma_f32 v[70:71], v[70:71], v[62:63], v[104:105]
	v_pk_fma_f32 v[72:73], v[72:73], v[56:57], v[102:103]
	v_pk_mul_f32 v[56:57], v[66:67], v[74:75] op_sel_hi:[1,0]
	v_pk_mul_f32 v[62:63], v[68:69], v[74:75] op_sel_hi:[1,0]
	s_waitcnt vmcnt(14)
	v_and_b32_e32 v69, 0xffff0000, v125
	v_lshlrev_b32_e32 v66, 16, v124
	v_and_b32_e32 v67, 0xffff0000, v124
	v_lshlrev_b32_e32 v68, 16, v125
	s_waitcnt lgkmcnt(0)
	v_pk_fma_f32 v[66:67], v[62:63], v[82:83], v[66:67]
	v_pk_fma_f32 v[68:69], v[56:57], v[84:85], v[68:69]
	global_store_dwordx4 v[64:65], v[66:69], off offset:320 sc1
	ds_read_b128 v[66:69], v139 offset:384
	global_store_dwordx4 v[64:65], v[70:73], off offset:256 sc1
	ds_read_b128 v[70:73], v139 offset:448
	v_pk_mul_f32 v[56:57], v[76:77], v[74:75] op_sel_hi:[1,0]
	v_pk_mul_f32 v[62:63], v[86:87], v[74:75] op_sel_hi:[1,0]
	s_waitcnt vmcnt(15)
	v_and_b32_e32 v77, 0xffff0000, v121
	v_lshlrev_b32_e32 v82, 16, v120
	v_and_b32_e32 v83, 0xffff0000, v120
	v_lshlrev_b32_e32 v76, 16, v121
	s_waitcnt lgkmcnt(1)
	v_pk_fma_f32 v[66:67], v[62:63], v[66:67], v[82:83]
	v_pk_fma_f32 v[68:69], v[56:57], v[68:69], v[76:77]
	global_store_dwordx4 v[64:65], v[66:69], off offset:384 sc1
	v_pk_mul_f32 v[56:57], v[88:89], v[74:75] op_sel_hi:[1,0]
	v_pk_mul_f32 v[62:63], v[90:91], v[74:75] op_sel_hi:[1,0]
	s_waitcnt vmcnt(15)
	v_and_b32_e32 v69, 0xffff0000, v117
	v_lshlrev_b32_e32 v66, 16, v116
	v_and_b32_e32 v67, 0xffff0000, v116
	v_lshlrev_b32_e32 v68, 16, v117
	s_waitcnt lgkmcnt(0)
	v_pk_fma_f32 v[66:67], v[62:63], v[70:71], v[66:67]
	v_pk_fma_f32 v[68:69], v[56:57], v[72:73], v[68:69]
	global_store_dwordx4 v[64:65], v[66:69], off offset:448 sc1
; DEVINL float bflo(unsigned u) { return __uint_as_float(u << 16); }
; DEVINL float bfhi(unsigned u) { return __uint_as_float(u & 0xffff0000u); }
; #define LDX1(mi_, buf_) { const int tk_ = s_tok[16 * (mi_) + lr2]; const bf16_t* xr_ = X1B + (size_t)(tk_ < 0 ? 0 : tk_) * DM + 128 * wv + 4 * g2; \
;                 _Pragma("unroll") for (int c_ = 0; c_ < 8; ++c_) xb[buf_][c_] = *(const u32x2*)(xr_ + 16 * c_); }
; DEVINL void phase5(const Params& P, unsigned char* smem) {
;     ...
;             for (int mi = 0; mi < 5; ++mi) {
;                 if (mi + 1 < 5) LDX1(mi + 1, (mi + 1) & 1)
;                 const int tok = s_tok[16 * mi + lr2];
;                 float qs = 0.f;
; #pragma unroll
;                 for (int w2 = 0; w2 < 8; ++w2) qs += s_part[w2 * 80 + 16 * mi + lr2];
;                 const float rstd = rsqrtf(qs * (1.f / DM) + EPS);
;                 const float* gfr = s_gfp + ((tok >> 13) & 1) * 1024 + 128 * wv + 4 * g2;
;                 float* orow = P.out + (size_t)(tok < 0 ? 0 : tok) * DM + 128 * wv + 4 * g2;
; #pragma unroll
;                 for (int c = 0; c < 8; ++c) {
;                     const f32x4 yv = c < 4 ? (f32x4){bflo(ypk[c & 3][mi].x), bfhi(ypk[c & 3][mi].x), bflo(ypk[c & 3][mi].y), bfhi(ypk[c & 3][mi].y)} : acc[c & 3][mi];
;                     const u32x2 xv = xb[mi & 1][c];
;                     const f32x4 x1 = {bflo(xv.x), bfhi(xv.x), bflo(xv.y), bfhi(xv.y)};
;                     const f32x4 gg = *(const f32x4*)(gfr + 16 * c);
;                     if (tok >= 0) *(f32x4*)(orow + 16 * c) = x1 + gg * (yv * rstd);
;                 }
.LBB0_736:
	s_or_b64 exec, exec, s[0:1]
	ds_read2_b32 v[76:77], v175 offset0:48 offset1:64
	s_waitcnt lgkmcnt(0)
	v_max_i32_e32 v194, 0, v77
	v_lshlrev_b64 v[56:57], 11, v[194:195]
	v_lshl_add_u64 v[82:83], v[92:93], 0, v[56:57]
	global_load_dwordx2 v[74:75], v[82:83], off
	global_load_dwordx2 v[72:73], v[82:83], off offset:32
	global_load_dwordx2 v[70:71], v[82:83], off offset:64
	global_load_dwordx2 v[68:69], v[82:83], off offset:96
	global_load_dwordx2 v[66:67], v[82:83], off offset:128
	global_load_dwordx2 v[64:65], v[82:83], off offset:160
	global_load_dwordx2 v[62:63], v[82:83], off offset:192
	global_load_dwordx2 v[56:57], v[82:83], off offset:224
	v_cmp_lt_i32_e32 vcc, -1, v76
	s_and_saveexec_b64 s[0:1], vcc
	s_cbranch_execz .LBB0_738
	ds_read2_b32 v[82:83], v177 offset0:48 offset1:128
	v_cvt_pk_bf16_f32 v90, v58, v59
	ds_read2_b32 v[58:59], v156 offset0:80 offset1:160
	v_cvt_pk_bf16_f32 v88, v78, v79
	ds_read2_b32 v[78:79], v176 offset0:112 offset1:192
	s_waitcnt lgkmcnt(2)
	v_add_f32_e32 v77, 0, v82
	v_cvt_pk_bf16_f32 v89, v80, v81
	v_add_f32_e32 v77, v77, v83
	ds_read2_b32 v[80:81], v126 offset0:16 offset1:96
	s_waitcnt lgkmcnt(2)
	v_add_f32_e32 v58, v77, v58
	v_add_f32_e32 v58, v58, v59
	s_waitcnt lgkmcnt(1)
	v_add_f32_e32 v58, v58, v78
	v_add_f32_e32 v58, v58, v79
	s_waitcnt lgkmcnt(0)
	v_add_f32_e32 v58, v58, v80
	v_add_f32_e32 v58, v58, v81
	v_fmamk_f32 v58, v58, 0x3a800000, v221
	v_mul_f32_e32 v59, 0x4b800000, v58
	v_cmp_gt_f32_e32 vcc, s48, v58
	v_cvt_pk_bf16_f32 v92, v42, v43
	v_cvt_pk_bf16_f32 v45, v44, v45
	v_cndmask_b32_e32 v58, v58, v59, vcc
	v_rsq_f32_e32 v58, v58
	v_cvt_pk_bf16_f32 v84, v98, v99
	v_cvt_pk_bf16_f32 v85, v100, v101
	v_cvt_pk_bf16_f32 v91, v60, v61
	v_mul_f32_e32 v42, 0x45800000, v58
	v_cndmask_b32_e32 v44, v58, v42, vcc
	v_lshrrev_b32_e32 v58, 1, v76
	v_and_b32_e32 v58, 0x1000, v58
	v_add_u32_e32 v93, v174, v58
	v_lshlrev_b32_e32 v58, 16, v84
	v_and_b32_e32 v59, 0xffff0000, v84
	v_lshlrev_b32_e32 v60, 16, v85
	v_and_b32_e32 v61, 0xffff0000, v85
	v_pk_mul_f32 v[80:81], v[44:45], v[58:59] op_sel_hi:[0,1]
	v_pk_mul_f32 v[82:83], v[44:45], v[60:61] op_sel_hi:[0,1]
	ds_read_b128 v[58:61], v93
	v_mov_b32_e32 v77, v195
	v_lshlrev_b64 v[42:43], 12, v[76:77]
	ds_read_b128 v[76:79], v93 offset:64
	v_lshl_add_u64 v[42:43], s[12:13], 0, v[42:43]
	s_waitcnt vmcnt(15)
	v_and_b32_e32 v85, 0xffff0000, v119
	v_lshlrev_b32_e32 v86, 16, v118
	v_and_b32_e32 v87, 0xffff0000, v118
	v_lshlrev_b32_e32 v84, 16, v119
	v_lshl_add_u64 v[42:43], v[54:55], 2, v[42:43]
	s_waitcnt lgkmcnt(1)
	v_pk_fma_f32 v[60:61], v[60:61], v[82:83], v[84:85]
	v_pk_fma_f32 v[58:59], v[58:59], v[80:81], v[86:87]
	global_store_dwordx4 v[42:43], v[58:61], off sc1
	s_waitcnt vmcnt(15)
	v_and_b32_e32 v81, 0xffff0000, v115
	v_lshlrev_b32_e32 v82, 16, v114
	v_lshlrev_b32_e32 v58, 16, v88
	v_and_b32_e32 v59, 0xffff0000, v88
	v_lshlrev_b32_e32 v60, 16, v89
	v_and_b32_e32 v61, 0xffff0000, v89
	v_pk_mul_f32 v[58:59], v[44:45], v[58:59] op_sel_hi:[0,1]
	v_pk_mul_f32 v[60:61], v[44:45], v[60:61] op_sel_hi:[0,1]
	v_and_b32_e32 v83, 0xffff0000, v114
	v_lshlrev_b32_e32 v80, 16, v115
	s_waitcnt lgkmcnt(0)
	v_pk_fma_f32 v[60:61], v[78:79], v[60:61], v[80:81]
	v_pk_fma_f32 v[58:59], v[76:77], v[58:59], v[82:83]
	global_store_dwordx4 v[42:43], v[58:61], off offset:64 sc1
	ds_read_b128 v[76:79], v93 offset:192
	s_waitcnt vmcnt(15)
	v_and_b32_e32 v85, 0xffff0000, v113
	v_lshlrev_b32_e32 v58, 16, v90
	v_and_b32_e32 v59, 0xffff0000, v90
	v_lshlrev_b32_e32 v60, 16, v91
	v_and_b32_e32 v61, 0xffff0000, v91
	v_pk_mul_f32 v[80:81], v[44:45], v[58:59] op_sel_hi:[0,1]
	v_pk_mul_f32 v[82:83], v[44:45], v[60:61] op_sel_hi:[0,1]
	ds_read_b128 v[58:61], v93 offset:128
	v_lshlrev_b32_e32 v86, 16, v112
	v_and_b32_e32 v87, 0xffff0000, v112
	v_lshlrev_b32_e32 v84, 16, v113
	v_pk_mul_f32 v[46:47], v[46:47], v[44:45] op_sel_hi:[1,0]
	s_waitcnt lgkmcnt(0)
	v_pk_fma_f32 v[60:61], v[60:61], v[82:83], v[84:85]
	v_pk_fma_f32 v[58:59], v[58:59], v[80:81], v[86:87]
	global_store_dwordx4 v[42:43], v[58:61], off offset:128 sc1
	s_waitcnt vmcnt(15)
	v_and_b32_e32 v81, 0xffff0000, v111
	v_lshlrev_b32_e32 v82, 16, v110
	v_lshlrev_b32_e32 v58, 16, v45
	v_and_b32_e32 v59, 0xffff0000, v45
	v_lshlrev_b32_e32 v60, 16, v92
	v_and_b32_e32 v61, 0xffff0000, v92
	v_pk_mul_f32 v[58:59], v[44:45], v[58:59] op_sel_hi:[0,1]
	v_pk_mul_f32 v[60:61], v[44:45], v[60:61] op_sel_hi:[0,1]
	v_and_b32_e32 v83, 0xffff0000, v110
	v_lshlrev_b32_e32 v80, 16, v111
	v_pk_fma_f32 v[60:61], v[78:79], v[60:61], v[80:81]
	v_pk_fma_f32 v[58:59], v[76:77], v[58:59], v[82:83]
	v_pk_mul_f32 v[76:77], v[34:35], v[44:45] op_sel_hi:[1,0]
	v_pk_mul_f32 v[78:79], v[36:37], v[44:45] op_sel_hi:[1,0]
	ds_read_b128 v[34:37], v93 offset:256
	global_store_dwordx4 v[42:43], v[58:61], off offset:192 sc1
	ds_read_b128 v[58:61], v93 offset:320
	s_waitcnt vmcnt(15)
	v_and_b32_e32 v81, 0xffff0000, v109
	v_lshlrev_b32_e32 v82, 16, v108
	v_and_b32_e32 v83, 0xffff0000, v108
	v_lshlrev_b32_e32 v80, 16, v109
	s_waitcnt lgkmcnt(1)
	v_pk_fma_f32 v[34:35], v[34:35], v[78:79], v[82:83]
	v_pk_fma_f32 v[36:37], v[36:37], v[76:77], v[80:81]
	global_store_dwordx4 v[42:43], v[34:37], off offset:256 sc1
	v_pk_mul_f32 v[48:49], v[48:49], v[44:45] op_sel_hi:[1,0]
	s_nop 0
	v_pk_mul_f32 v[36:37], v[38:39], v[44:45] op_sel_hi:[1,0]
	v_pk_mul_f32 v[34:35], v[40:41], v[44:45] op_sel_hi:[1,0]
	s_waitcnt vmcnt(15)
	v_and_b32_e32 v39, 0xffff0000, v107
	v_lshlrev_b32_e32 v40, 16, v106
	v_and_b32_e32 v41, 0xffff0000, v106
	v_lshlrev_b32_e32 v38, 16, v107
	s_waitcnt lgkmcnt(0)
	v_pk_fma_f32 v[34:35], v[34:35], v[58:59], v[40:41]
	v_pk_fma_f32 v[36:37], v[36:37], v[60:61], v[38:39]
	global_store_dwordx4 v[42:43], v[34:37], off offset:320 sc1
	ds_read_b128 v[34:37], v93 offset:384
	ds_read_b128 v[38:41], v93 offset:448
	s_waitcnt vmcnt(15)
	v_and_b32_e32 v59, 0xffff0000, v97
	v_lshlrev_b32_e32 v60, 16, v96
	v_and_b32_e32 v61, 0xffff0000, v96
	v_lshlrev_b32_e32 v58, 16, v97
	s_waitcnt lgkmcnt(1)
	v_pk_fma_f32 v[34:35], v[48:49], v[34:35], v[60:61]
	v_pk_fma_f32 v[36:37], v[46:47], v[36:37], v[58:59]
	global_store_dwordx4 v[42:43], v[34:37], off offset:384 sc1
	s_waitcnt vmcnt(15)
	v_lshlrev_b32_e32 v46, 16, v94
	v_and_b32_e32 v47, 0xffff0000, v94
	v_pk_mul_f32 v[36:37], v[50:51], v[44:45] op_sel_hi:[1,0]
	v_pk_mul_f32 v[34:35], v[52:53], v[44:45] op_sel_hi:[1,0]
	v_and_b32_e32 v45, 0xffff0000, v95
	v_lshlrev_b32_e32 v44, 16, v95
	s_waitcnt lgkmcnt(0)
	v_pk_fma_f32 v[34:35], v[34:35], v[38:39], v[46:47]
	v_pk_fma_f32 v[36:37], v[36:37], v[40:41], v[44:45]
	global_store_dwordx4 v[42:43], v[34:37], off offset:448 sc1
; DEVINL float bflo(unsigned u) { return __uint_as_float(u << 16); }
; DEVINL float bfhi(unsigned u) { return __uint_as_float(u & 0xffff0000u); }
; #define LDX1(mi_, buf_) { const int tk_ = s_tok[16 * (mi_) + lr2]; const bf16_t* xr_ = X1B + (size_t)(tk_ < 0 ? 0 : tk_) * DM + 128 * wv + 4 * g2; \
;                 _Pragma("unroll") for (int c_ = 0; c_ < 8; ++c_) xb[buf_][c_] = *(const u32x2*)(xr_ + 16 * c_); }
; DEVINL void phase5(const Params& P, unsigned char* smem) {
;     ...
;             for (int mi = 0; mi < 5; ++mi) {
;                 if (mi + 1 < 5) LDX1(mi + 1, (mi + 1) & 1)
;                 const int tok = s_tok[16 * mi + lr2];
;                 float qs = 0.f;
; #pragma unroll
;                 for (int w2 = 0; w2 < 8; ++w2) qs += s_part[w2 * 80 + 16 * mi + lr2];
;                 const float rstd = rsqrtf(qs * (1.f / DM) + EPS);
;                 const float* gfr = s_gfp + ((tok >> 13) & 1) * 1024 + 128 * wv + 4 * g2;
;                 float* orow = P.out + (size_t)(tok < 0 ? 0 : tok) * DM + 128 * wv + 4 * g2;
; #pragma unroll
;                 for (int c = 0; c < 8; ++c) {
;                     const f32x4 yv = c < 4 ? (f32x4){bflo(ypk[c & 3][mi].x), bfhi(ypk[c & 3][mi].x), bflo(ypk[c & 3][mi].y), bfhi(ypk[c & 3][mi].y)} : acc[c & 3][mi];
;                     const u32x2 xv = xb[mi & 1][c];
;                     const f32x4 x1 = {bflo(xv.x), bfhi(xv.x), bflo(xv.y), bfhi(xv.y)};
;                     const f32x4 gg = *(const f32x4*)(gfr + 16 * c);
;                     if (tok >= 0) *(f32x4*)(orow + 16 * c) = x1 + gg * (yv * rstd);
;                 }
.LBB0_738:
	s_or_b64 exec, exec, s[0:1]
	ds_read_b32 v194, v175 offset:256
	s_waitcnt lgkmcnt(0)
	v_cmp_lt_i32_e32 vcc, -1, v194
	s_and_saveexec_b64 s[0:1], vcc
	s_cbranch_execz .LBB0_691
	v_cvt_pk_bf16_f32 v35, v2, v3
	ds_read2_b32 v[2:3], v177 offset0:64 offset1:144
	v_cvt_pk_bf16_f32 v34, v4, v5
	ds_read2_b32 v[4:5], v156 offset0:96 offset1:176
	v_cvt_pk_bf16_f32 v39, v6, v7
	ds_read2_b32 v[6:7], v176 offset0:128 offset1:208
	s_waitcnt lgkmcnt(2)
	v_add_f32_e32 v2, 0, v2
	v_cvt_pk_bf16_f32 v38, v8, v9
	v_add_f32_e32 v8, v2, v3
	ds_read2_b32 v[2:3], v126 offset0:32 offset1:112
	s_waitcnt lgkmcnt(2)
	v_add_f32_e32 v4, v8, v4
	v_add_f32_e32 v4, v4, v5
	s_waitcnt lgkmcnt(1)
	v_add_f32_e32 v4, v4, v6
	v_add_f32_e32 v4, v4, v7
	s_waitcnt lgkmcnt(0)
	v_add_f32_e32 v2, v4, v2
	v_add_f32_e32 v2, v2, v3
	v_fmamk_f32 v2, v2, 0x3a800000, v221
	v_mul_f32_e32 v3, 0x4b800000, v2
	v_cmp_gt_f32_e32 vcc, s48, v2
	v_lshrrev_b32_e32 v4, 1, v194
	v_and_b32_e32 v4, 0x1000, v4
	v_cndmask_b32_e32 v2, v2, v3, vcc
	v_rsq_f32_e32 v2, v2
	v_cvt_pk_bf16_f32 v15, v14, v15
	v_add_u32_e32 v43, v174, v4
	v_lshlrev_b32_e32 v4, 16, v34
	v_mul_f32_e32 v3, 0x45800000, v2
	v_cndmask_b32_e32 v14, v2, v3, vcc
	v_and_b32_e32 v5, 0xffff0000, v34
	v_lshlrev_b32_e32 v6, 16, v35
	v_and_b32_e32 v7, 0xffff0000, v35
	v_cvt_pk_bf16_f32 v41, v24, v25
	v_pk_mul_f32 v[8:9], v[14:15], v[4:5] op_sel_hi:[0,1]
	v_pk_mul_f32 v[24:25], v[14:15], v[6:7] op_sel_hi:[0,1]
	ds_read_b128 v[4:7], v43
	v_cvt_pk_bf16_f32 v40, v20, v21
	v_cvt_pk_bf16_f32 v42, v22, v23
	v_lshlrev_b64 v[2:3], 12, v[194:195]
	ds_read_b128 v[20:23], v43 offset:64
	v_lshl_add_u64 v[2:3], s[12:13], 0, v[2:3]
	s_waitcnt vmcnt(7)
	v_and_b32_e32 v35, 0xffff0000, v75
	v_lshlrev_b32_e32 v36, 16, v74
	v_and_b32_e32 v37, 0xffff0000, v74
	v_lshlrev_b32_e32 v34, 16, v75
	v_lshl_add_u64 v[2:3], v[54:55], 2, v[2:3]
	s_waitcnt lgkmcnt(1)
	v_pk_fma_f32 v[6:7], v[6:7], v[24:25], v[34:35]
	v_pk_fma_f32 v[4:5], v[4:5], v[8:9], v[36:37]
	global_store_dwordx4 v[2:3], v[4:7], off sc1
	s_waitcnt vmcnt(7)
	v_and_b32_e32 v9, 0xffff0000, v73
	v_lshlrev_b32_e32 v24, 16, v72
	v_lshlrev_b32_e32 v4, 16, v38
	v_and_b32_e32 v5, 0xffff0000, v38
	v_lshlrev_b32_e32 v6, 16, v39
	v_and_b32_e32 v7, 0xffff0000, v39
	v_pk_mul_f32 v[4:5], v[14:15], v[4:5] op_sel_hi:[0,1]
	v_pk_mul_f32 v[6:7], v[14:15], v[6:7] op_sel_hi:[0,1]
	v_and_b32_e32 v25, 0xffff0000, v72
	v_lshlrev_b32_e32 v8, 16, v73
	s_waitcnt lgkmcnt(0)
	v_pk_fma_f32 v[6:7], v[22:23], v[6:7], v[8:9]
	v_pk_fma_f32 v[4:5], v[20:21], v[4:5], v[24:25]
	global_store_dwordx4 v[2:3], v[4:7], off offset:64 sc1
	ds_read_b128 v[20:23], v43 offset:192
	s_waitcnt vmcnt(7)
	v_and_b32_e32 v35, 0xffff0000, v71
	v_lshlrev_b32_e32 v4, 16, v40
	v_and_b32_e32 v5, 0xffff0000, v40
	v_lshlrev_b32_e32 v6, 16, v15
	v_and_b32_e32 v7, 0xffff0000, v15
	v_pk_mul_f32 v[8:9], v[14:15], v[4:5] op_sel_hi:[0,1]
	v_pk_mul_f32 v[24:25], v[14:15], v[6:7] op_sel_hi:[0,1]
	ds_read_b128 v[4:7], v43 offset:128
	v_lshlrev_b32_e32 v36, 16, v70
	v_and_b32_e32 v37, 0xffff0000, v70
	v_lshlrev_b32_e32 v34, 16, v71
	v_pk_mul_f32 v[12:13], v[12:13], v[14:15] op_sel_hi:[1,0]
	s_waitcnt lgkmcnt(0)
	v_pk_fma_f32 v[6:7], v[6:7], v[24:25], v[34:35]
	v_pk_fma_f32 v[4:5], v[4:5], v[8:9], v[36:37]
	global_store_dwordx4 v[2:3], v[4:7], off offset:128 sc1
	s_waitcnt vmcnt(7)
	v_and_b32_e32 v9, 0xffff0000, v69
	v_lshlrev_b32_e32 v24, 16, v68
	v_lshlrev_b32_e32 v4, 16, v41
	v_and_b32_e32 v5, 0xffff0000, v41
	v_lshlrev_b32_e32 v6, 16, v42
	v_and_b32_e32 v7, 0xffff0000, v42
	v_pk_mul_f32 v[4:5], v[14:15], v[4:5] op_sel_hi:[0,1]
	v_pk_mul_f32 v[6:7], v[14:15], v[6:7] op_sel_hi:[0,1]
	v_and_b32_e32 v25, 0xffff0000, v68
	v_lshlrev_b32_e32 v8, 16, v69
	v_pk_fma_f32 v[6:7], v[22:23], v[6:7], v[8:9]
	v_pk_fma_f32 v[4:5], v[20:21], v[4:5], v[24:25]
	global_store_dwordx4 v[2:3], v[4:7], off offset:192 sc1
	ds_read_b128 v[4:7], v43 offset:256
	v_pk_mul_f32 v[20:21], v[10:11], v[14:15] op_sel_hi:[1,0]
	ds_read_b128 v[8:11], v43 offset:320
	s_waitcnt vmcnt(7)
	v_and_b32_e32 v23, 0xffff0000, v67
	v_lshlrev_b32_e32 v24, 16, v66
	v_and_b32_e32 v25, 0xffff0000, v66
	v_lshlrev_b32_e32 v22, 16, v67
	s_waitcnt lgkmcnt(1)
	v_pk_fma_f32 v[4:5], v[4:5], v[12:13], v[24:25]
	v_pk_fma_f32 v[6:7], v[6:7], v[20:21], v[22:23]
	global_store_dwordx4 v[2:3], v[4:7], off offset:256 sc1
	s_waitcnt vmcnt(7)
	v_and_b32_e32 v13, 0xffff0000, v65
	v_lshlrev_b32_e32 v12, 16, v65
	v_pk_mul_f32 v[6:7], v[16:17], v[14:15] op_sel_hi:[1,0]
	v_pk_mul_f32 v[4:5], v[18:19], v[14:15] op_sel_hi:[1,0]
	v_lshlrev_b32_e32 v16, 16, v64
	v_and_b32_e32 v17, 0xffff0000, v64
	s_waitcnt lgkmcnt(0)
	v_pk_fma_f32 v[4:5], v[4:5], v[8:9], v[16:17]
	v_pk_fma_f32 v[6:7], v[6:7], v[10:11], v[12:13]
	global_store_dwordx4 v[2:3], v[4:7], off offset:320 sc1
	ds_read_b128 v[4:7], v43 offset:384
	ds_read_b128 v[8:11], v43 offset:448
	v_pk_mul_f32 v[12:13], v[26:27], v[14:15] op_sel_hi:[1,0]
	v_pk_mul_f32 v[16:17], v[28:29], v[14:15] op_sel_hi:[1,0]
	s_waitcnt vmcnt(7)
	v_and_b32_e32 v19, 0xffff0000, v63
	v_lshlrev_b32_e32 v20, 16, v62
	v_and_b32_e32 v21, 0xffff0000, v62
	v_lshlrev_b32_e32 v18, 16, v63
	s_waitcnt lgkmcnt(1)
	v_pk_fma_f32 v[4:5], v[16:17], v[4:5], v[20:21]
	v_pk_fma_f32 v[6:7], v[12:13], v[6:7], v[18:19]
	global_store_dwordx4 v[2:3], v[4:7], off offset:384 sc1
	s_waitcnt vmcnt(7)
	v_and_b32_e32 v13, 0xffff0000, v57
	v_lshlrev_b32_e32 v12, 16, v57
	v_pk_mul_f32 v[6:7], v[30:31], v[14:15] op_sel_hi:[1,0]
	v_pk_mul_f32 v[4:5], v[32:33], v[14:15] op_sel_hi:[1,0]
	v_lshlrev_b32_e32 v14, 16, v56
	v_and_b32_e32 v15, 0xffff0000, v56
	s_waitcnt lgkmcnt(0)
	v_pk_fma_f32 v[4:5], v[4:5], v[8:9], v[14:15]
	v_pk_fma_f32 v[6:7], v[6:7], v[10:11], v[12:13]
	global_store_dwordx4 v[2:3], v[4:7], off offset:448 sc1
	s_branch .LBB0_691
